# speedup vs baseline: 1.0113x; 1.0113x over previous
_Z6k_gemmPKfS0_PK15HIP_vector_typeIjLj4EEPDF16_PKh:
	s_load_dwordx4 s[20:23], s[0:1], 0x0
	s_load_dwordx4 s[4:7], s[0:1], 0x10
	s_load_dwordx2 s[38:39], s[0:1], 0x20
	v_readfirstlane_b32 s8, v0
	v_and_b32_e32 v1, 63, v0
	s_nop 3
	s_lshr_b32 s8, s8, 6
	s_and_b32 s40, s2, 7
	s_lshr_b32 s41, s2, 3
	s_mul_i32 s18, s40, 0x187
	s_add_u32 s19, s18, 0x187
	s_min_u32 s19, s19, 0xc35
	s_sub_u32 s33, s19, s18
	s_sub_u32 s33, s33, 0x180
	s_lshl_b32 s33, s33, 2
	s_cmp_lt_u32 s41, s33
	s_cselect_b32 s44, 7, 6
	s_lshr_b32 s45, s41, 2
	s_add_u32 s45, s45, s18
	s_add_u32 s45, s45, 0x180
	s_lshl_b32 s45, s45, 4
	s_and_b32 s46, s41, 3
	s_lshl_b32 s46, s46, 2
	s_add_u32 s47, s45, s46
	s_mul_i32 s45, s47, 0x4b0
	s_lshl_b32 s46, s47, 8
	s_add_i32 s18, s18, s41
	s_cmp_eq_u32 s8, 0
	s_cselect_b32 s9, s44, 6
	s_add_i32 s11, s44, 4
	s_lshl_b32 s18, s18, 4
	s_lshl_b32 s19, s8, 2
	s_add_i32 s33, s18, s19
	s_mul_i32 s12, s33, 0x4b0
	s_lshl_b32 s32, s18, 8
	s_sub_u32 s32, s32, 0x100000
	s_mov_b32 s10, 0
	v_lshl_add_u32 v253, v1, 10, s33
	v_mov_b32_e32 v254, s47
	v_cmp_eq_u32_e32 vcc, 6, v1
	s_nop 1
	v_cndmask_b32_e32 v253, v253, v254, vcc
	v_mov_b32_e32 v247, 0
	v_cmp_gt_i32_e32 vcc, s9, v1
	s_mov_b32 s18, 0xc350
	v_cmp_gt_i32_e64 s[36:37], s18, v253
	s_and_b64 vcc, vcc, s[36:37]
	s_waitcnt lgkmcnt(0)
	s_and_saveexec_b64 s[36:37], vcc
	global_load_dword v247, v253, s[38:39]
	s_mov_b64 exec, s[36:37]
	s_mov_b32 s24, s22
	s_and_b32 s25, s23, 0xffff
	s_mov_b32 s26, 0x3938700
	s_mov_b32 s27, 0x20000
	s_and_b32 s21, s21, 0xffff
	s_mov_b32 s22, 0x3938700
	s_mov_b32 s23, 0x20000
	s_mov_b32 s28, s6
	s_and_b32 s29, s7, 0xffff
	s_mov_b32 s30, 0xc35000
	s_mov_b32 s31, 0x20000
	v_lshlrev_b32_e32 v238, 4, v1
	buffer_load_dwordx4 v[138:141], v238, s[20:23], s12 offen nt
	buffer_load_dwordx4 v[142:145], v238, s[24:27], s12 offen nt
	v_mul_u32_u24_e32 v253, 0x1746, v1
	v_lshrrev_b32_e32 v253, 16, v253
	v_min_u32_e32 v253, 3, v253
	v_mul_u32_u24_e32 v254, 11, v253
	v_sub_u32_e32 v254, v1, v254
	v_lshlrev_b32_e32 v240, 3, v253
	v_mul_u32_u24_e32 v249, 0x4b0, v253
	v_lshl_add_u32 v249, v254, 4, v249
	v_add_u32_e32 v249, 0x400, v249
	v_mov_b32_e32 v255, 0x80000000
	v_cmp_gt_u32_e64 s[34:35], 44, v1
	s_nop 1
	v_cndmask_b32_e64 v239, v255, v249, s[34:35]
	v_lshl_add_u32 v250, s8, 2, v253
	v_mul_u32_u24_e32 v250, 0x4e0, v250
	v_lshl_add_u32 v250, v254, 3, v250
	v_add_u32_e32 v242, 0x200, v250
	s_mul_i32 s18, s8, 0x1380
	v_lshl_add_u32 v241, v1, 3, s18
	v_and_b32_e32 v249, 15, v1
	v_lshrrev_b32_e32 v250, 4, v1
	v_mul_u32_u24_e32 v243, 0x4e0, v249
	v_lshl_add_u32 v243, v250, 4, v243
	v_mul_u32_u24_e32 v244, 0x440, v250
	v_lshl_add_u32 v244, v249, 1, v244
	s_lshl_b32 s18, s8, 6
	s_add_i32 s18, s18, 39936
	v_add_u32_e32 v244, s18, v244
	v_lshrrev_b32_e32 v249, 4, v0
	v_and_b32_e32 v250, 15, v0
	v_mul_u32_u24_e32 v245, 0x110, v249
	v_lshl_add_u32 v245, v250, 4, v245
	v_add_u32_e32 v245, 39936, v245
	v_lshlrev_b32_e32 v246, 8, v249
	v_lshl_add_u32 v246, v250, 4, v246
	s_lshl_b32 s18, s8, 12
	s_add_i32 s18, s18, 48640
	v_lshl_add_u32 v248, v1, 4, s18
	v_cmp_gt_u32_e32 vcc, 32, v0
	s_and_saveexec_b64 s[36:37], vcc
	v_mul_u32_u24_e32 v251, 0x4e00, v249
	v_mul_u32_u24_e32 v252, 0x4e0, v250
	v_add_u32_e32 v254, v251, v252
	v_mov_b32_e32 v250, 0
	v_mov_b32_e32 v251, 0
	v_mov_b32_e32 v252, 0
	v_mov_b32_e32 v253, 0
	ds_write_b128 v254, v[250:253] offset:1200
	s_mov_b64 exec, s[36:37]
	s_lshl_b32 s18, s8, 11
	v_lshl_add_u32 v253, v1, 4, s18
	v_add_u32_e32 v254, 0x22000, v253
	global_load_dwordx4 v[178:181], v254, s[4:5]
	global_load_dwordx4 v[182:185], v254, s[4:5] offset:1024
	v_add_u32_e32 v254, 0x2000, v254
	global_load_dwordx4 v[186:189], v254, s[4:5]
	global_load_dwordx4 v[190:193], v254, s[4:5] offset:1024
	v_mov_b32_e32 v236, v253
	s_waitcnt vmcnt(6)
	v_readlane_b32 s13, v247, s10
	s_add_u32 s14, s12, 0x4b0
	s_add_u32 s15, s12, 0x960
	s_add_u32 s16, s12, 0xe10
	s_nop 1
	s_and_b32 s18, s13, 0xff
	s_cmp_eq_u32 s18, 1
	s_cselect_b32 s42, s12, 0x80000000
	s_and_b32 s18, s13, 0xff00
	s_cmp_eq_u32 s18, 0x100
	s_cselect_b32 s14, s14, 0x80000000
	s_and_b32 s18, s13, 0xff0000
	s_cmp_eq_u32 s18, 0x10000
	s_cselect_b32 s15, s15, 0x80000000
	s_and_b32 s18, s13, 0xff000000
	s_cmp_eq_u32 s18, 0x1000000
	s_cselect_b32 s16, s16, 0x80000000
	v_lshrrev_b32_e64 v249, v240, s13
	v_and_b32_e32 v249, 0xff, v249
	v_cmp_eq_u32_e32 vcc, 1, v249
	s_nop 1
	v_cndmask_b32_e32 v254, v255, v239, vcc
	buffer_load_dwordx4 v[146:149], v238, s[20:23], s14 offen nt
	buffer_load_dwordx4 v[150:153], v238, s[24:27], s14 offen nt
	buffer_load_dwordx4 v[154:157], v238, s[20:23], s15 offen nt
	buffer_load_dwordx4 v[158:161], v238, s[24:27], s15 offen nt
	buffer_load_dwordx4 v[162:165], v238, s[20:23], s16 offen nt
	buffer_load_dwordx4 v[166:169], v238, s[24:27], s16 offen nt
	buffer_load_dwordx4 v[170:173], v254, s[20:23], s12 offen nt
	buffer_load_dwordx4 v[174:177], v254, s[24:27], s12 offen nt
	s_add_u32 s12, s12, 0x12c000
	s_add_u32 s32, s32, 0x40000
	s_mov_b32 s19, 0x80000000
	buffer_store_dwordx4 v[226:229], v246, s[28:31], s19 offen nt
	s_mov_b32 s10, 1
	global_load_dwordx4 v[2:5], v236, s[4:5]
	global_load_dwordx4 v[6:9], v236, s[4:5] offset:1024
	v_add_u32_e32 v236, 0x2000, v236
	global_load_dwordx4 v[10:13], v236, s[4:5]
	global_load_dwordx4 v[14:17], v236, s[4:5] offset:1024
	v_add_u32_e32 v236, 0x2000, v236
	global_load_dwordx4 v[18:21], v236, s[4:5]
	global_load_dwordx4 v[22:25], v236, s[4:5] offset:1024
	v_add_u32_e32 v236, 0x2000, v236
	global_load_dwordx4 v[26:29], v236, s[4:5]
	global_load_dwordx4 v[30:33], v236, s[4:5] offset:1024
	v_add_u32_e32 v236, 0x2000, v236
	global_load_dwordx4 v[34:37], v236, s[4:5]
	global_load_dwordx4 v[38:41], v236, s[4:5] offset:1024
	v_add_u32_e32 v236, 0x2000, v236
	global_load_dwordx4 v[42:45], v236, s[4:5]
	global_load_dwordx4 v[46:49], v236, s[4:5] offset:1024
	v_add_u32_e32 v236, 0x2000, v236
	global_load_dwordx4 v[50:53], v236, s[4:5]
	global_load_dwordx4 v[54:57], v236, s[4:5] offset:1024
	v_add_u32_e32 v236, 0x2000, v236
	global_load_dwordx4 v[58:61], v236, s[4:5]
	global_load_dwordx4 v[62:65], v236, s[4:5] offset:1024
	v_add_u32_e32 v236, 0x2000, v236
	global_load_dwordx4 v[66:69], v236, s[4:5]
	global_load_dwordx4 v[70:73], v236, s[4:5] offset:1024
	v_add_u32_e32 v236, 0x2000, v236
	global_load_dwordx4 v[74:77], v236, s[4:5]
	global_load_dwordx4 v[78:81], v236, s[4:5] offset:1024
	v_add_u32_e32 v236, 0x2000, v236
	global_load_dwordx4 v[82:85], v236, s[4:5]
	global_load_dwordx4 v[86:89], v236, s[4:5] offset:1024
	v_add_u32_e32 v236, 0x2000, v236
	global_load_dwordx4 v[90:93], v236, s[4:5]
	global_load_dwordx4 v[94:97], v236, s[4:5] offset:1024
	v_add_u32_e32 v236, 0x2000, v236
	global_load_dwordx4 v[98:101], v236, s[4:5]
	global_load_dwordx4 v[102:105], v236, s[4:5] offset:1024
	v_add_u32_e32 v236, 0x2000, v236
	global_load_dwordx4 v[106:109], v236, s[4:5]
	global_load_dwordx4 v[110:113], v236, s[4:5] offset:1024
	v_add_u32_e32 v236, 0x2000, v236
	global_load_dwordx4 v[114:117], v236, s[4:5]
	global_load_dwordx4 v[118:121], v236, s[4:5] offset:1024
	v_add_u32_e32 v236, 0x2000, v236
	global_load_dwordx4 v[122:125], v236, s[4:5]
	global_load_dwordx4 v[126:129], v236, s[4:5] offset:1024
	v_add_u32_e32 v236, 0x2000, v236
	global_load_dwordx4 v[130:133], v236, s[4:5]
	global_load_dwordx4 v[134:137], v236, s[4:5] offset:1024
	s_waitcnt vmcnt(43)
	ds_write_b128 v248, v[178:181]
	ds_write_b128 v248, v[182:185] offset:1024
	ds_write_b128 v248, v[186:189] offset:2048
	ds_write_b128 v248, v[190:193] offset:3072
	s_waitcnt lgkmcnt(0)
	s_barrier
	s_branch .Lg_half1
